# speedup vs baseline: 1.0142x; 1.0142x over previous
.Lskip_tabld:
	v_readfirstlane_b32 s4, v156
	s_ashr_i32 s27, s4, 7
	s_lshl_b32 s0, s27, 1
	s_ashr_i32 s1, s0, 31
	s_lshl_b64 s[2:3], s[0:1], 13
	s_add_u32 s2, s8, s2
	s_addc_u32 s3, s9, s3
	s_add_u32 s28, s2, 0x18000
	s_addc_u32 s29, s3, 0
	v_lshlrev_b32_e32 v154, 4, v167
	v_lshl_add_u64 v[6:7], s[28:29], 0, v[154:155]
	v_or_b32_e32 v8, 0x800, v169
	v_add_co_u32_e32 v6, vcc, s23, v6
	v_lshlrev_b32_e32 v168, 1, v8
	s_nop 0
	v_addc_co_u32_e32 v7, vcc, 0, v7, vcc
	global_load_dwordx4 v[150:153], v154, s[28:29]
	global_load_dwordx4 v[146:149], v154, s[28:29] offset:1024
	global_load_dwordx4 v[142:145], v154, s[28:29] offset:2048
	global_load_dwordx4 v[138:141], v154, s[28:29] offset:3072
	global_load_dwordx4 v[126:129], v[6:7], off offset:1024
	global_load_dwordx4 v[122:125], v[6:7], off offset:2048
	global_load_dwordx4 v[134:137], v168, s[28:29]
	global_load_dwordx4 v[130:133], v[6:7], off offset:3072
	v_lshl_add_u64 v[6:7], s[2:3], 0, v[154:155]
	v_lshl_add_u64 v[8:9], v[6:7], 0, s[16:17]
	v_add_co_u32_e32 v6, vcc, 0x28000, v6
	s_nop 1
	v_addc_co_u32_e32 v7, vcc, 0, v7, vcc
	global_load_dwordx4 v[86:89], v[6:7], off
	global_load_dwordx4 v[82:85], v[8:9], off offset:1024
	v_lshl_add_u32 v166, v156, 2, v165
	s_cmp_lt_i32 s22, 0
	s_cbranch_scc0 .Lskip_stage0
	v_lshl_add_u32 v6, v156, 3, v1
	v_cmp_gt_i32_e32 vcc, 64, v156
	s_waitcnt vmcnt(11)
	ds_write_b64 v6, v[4:5]
	s_and_saveexec_b64 s[2:3], vcc
	s_cbranch_execz .LBB1_7
	s_waitcnt vmcnt(10)
	ds_write_b64 v6, v[2:3] offset:2048
.LBB1_7:
	s_or_b64 exec, exec, s[2:3]
	s_waitcnt vmcnt(10) lgkmcnt(0)
	s_barrier
.Lskip_stage0:
	s_ashr_i32 s2, s4, 6
	s_lshl_b32 s3, s2, 3
	s_and_b32 s5, s3, 8
	s_bfe_u32 s26, s2, 0x10001
	s_or_b32 s5, s26, s5
	s_lshl_b32 s26, s2, 9
	s_and_b32 s26, s26, 0x400
	s_lshl_b32 s5, s5, 4
	s_or_b32 s28, s5, s26
	v_lshrrev_b32_e32 v182, 5, v167
	v_bfe_u32 v2, v156, 4, 1
	v_bitop3_b32 v3, v182, v156, 1 bitop3:0x78
	v_lshlrev_b32_e32 v154, 2, v182
	v_xor_b32_e32 v3, v3, v2
	v_bitop3_b32 v4, v154, v156, 4 bitop3:0x78
	v_and_b32_e32 v5, 10, v156
	v_or3_b32 v3, v5, v4, v3
	s_lshl_b32 s5, s2, 4
	v_lshlrev_b32_e32 v3, 4, v3
	s_lshl_b32 s3, s2, 13
	s_and_b32 s29, s5, 16
	v_lshlrev_b32_e32 v170, 8, v182
	v_lshl_or_b32 v171, v2, 10, v3
	s_or_b32 s26, s29, s3
	v_bitop3_b32 v179, v171, s26, v170 bitop3:0x36
	s_or_b32 s5, s26, 0x280
	v_bitop3_b32 v178, v171, s5, v170 bitop3:0x36
	s_or_b32 s30, s3, 0x800
	s_or_b32 s33, s3, 0x1000
	s_or_b32 s29, s29, 64
	s_or_b32 s34, s29, s33
	v_bitop3_b32 v180, v171, s34, v170 bitop3:0x36
	s_or_b32 s29, s3, s29
	s_or_b32 s29, s29, 0x1280
	s_and_b32 s5, s2, 1
	s_lshl_b32 s31, s5, 4
	s_or_b32 s2, s31, s3
	v_bitop3_b32 v173, v171, s2, v170 bitop3:0x36
	v_bitop3_b32 v34, v156, 31, v156 bitop3:0xc
	v_lshrrev_b32_e32 v35, 4, v34
	v_bitop3_b32 v36, v34, v182, 1 bitop3:0x6c
	v_xor_b32_e32 v36, v36, v35
	v_bitop3_b32 v34, v34, v154, 4 bitop3:0x6c
	v_bitop3_b32 v37, v156, 10, 31 bitop3:8
	v_or3_b32 v34, v37, v34, v36
	v_lshlrev_b32_e32 v35, 10, v35
	v_lshlrev_b32_e32 v34, 4, v34
	v_or3_b32 v154, v35, v34, v170
	v_bitop3_b32 v172, s2, v154, v159 bitop3:0x36
	v_bitop3_b32 v176, v171, s29, v170 bitop3:0x36
	s_or_b32 s29, s31, s30
	s_or_b32 s29, s29, 0xa0
	v_bitop3_b32 v175, v171, s29, v170 bitop3:0x36
	s_or_b32 s29, s2, 0xaa0
	s_xor_b32 s29, s29, 0x80
	v_xor_b32_e32 v174, s29, v154
	s_or_b32 s29, s26, 0x18e0
	v_bitop3_b32 v181, v171, s29, v170 bitop3:0x36
	s_or_b32 s29, s26, 0x1a60
	v_bitop3_b32 v177, v171, s29, v170 bitop3:0x36
	s_or_b32 s29, s31, 64
	s_or_b32 s3, s3, s29
	s_mov_b32 s41, s3
	s_or_b32 s29, s29, s33
	s_mov_b32 s40, s29
	s_or_b32 s3, s2, 0x18e0
	s_mov_b32 s42, s3
	s_or_b32 s2, s2, 0x1ae0
	s_xor_b32 s2, s2, 0x80
	s_mov_b32 s43, s2
	s_lshr_b32 s38, s4, 1
	v_and_b32_e32 v26, 31, v167
	v_and_b32_e32 v27, 3, v167
	v_bfe_u32 v28, v167, 3, 1
	v_bfe_u32 v29, v167, 2, 1
	v_lshl_or_b32 v27, v28, 2, v27
	v_lshl_or_b32 v27, v29, 3, v27
	v_lshlrev_b32_e32 v32, 9, v182
	v_lshl_add_u32 v30, v27, 3, v32
	v_add_u32_e32 v30, 0x10000, v30
	v_lshl_add_u32 v31, v26, 3, v32
	v_add_u32_e32 v31, 0x10400, v31
	v_xor_b32_e32 v28, 31, v26
	v_lshl_add_u32 v28, v28, 3, v32
	v_add_u32_e32 v28, 0x10400, v28
	v_bfe_u32 v29, v167, 4, 1
	v_mul_u32_u24_e32 v29, 0x78, v29
	v_xor_b32_e32 v254, s38, v29
	v_or_b32_e32 v254, 0x10800, v254
	v_and_b32_e32 v33, 16, v167
	v_cmp_eq_u32_e32 vcc, 0, v33
	ds_read2_b64 v[66:69], v30 offset0:0 offset1:32
	ds_read2_b64 v[70:73], v30 offset0:16 offset1:48
	ds_read2_b64 v[198:201], v31 offset0:0 offset1:32
	ds_read2_b64 v[202:205], v28 offset0:0 offset1:32
	ds_read2_b64 v[206:209], v254 offset0:0 offset1:16
	ds_read2_b64 v[210:213], v254 offset0:32 offset1:48
	s_waitcnt lgkmcnt(0)
	v_cndmask_b32_e32 v74, v67, v66, vcc
	v_cndmask_b32_e32 v75, v69, v68, vcc
	v_cndmask_b32_e64 v76, v66, -v67, vcc
	v_cndmask_b32_e64 v77, v68, -v69, vcc
	v_cndmask_b32_e32 v78, v71, v70, vcc
	v_cndmask_b32_e32 v79, v73, v72, vcc
	v_cndmask_b32_e64 v80, v70, -v71, vcc
	v_cndmask_b32_e64 v81, v72, -v73, vcc
	v_cvt_pk_f16_f32 v190, v74, v75
	v_cvt_pk_f16_f32 v191, v74, v75
	v_cvt_pk_f16_f32 v192, v76, v77
	v_cvt_pk_f16_f32 v193, v76, v77
	v_cvt_pk_f16_f32 v194, v78, v79
	v_cvt_pk_f16_f32 v195, v78, v79
	v_cvt_pk_f16_f32 v196, v80, v81
	v_cvt_pk_f16_f32 v197, v80, v81
	v_mul_f32_e32 v66, v199, v207
	v_mul_f32_e32 v68, v199, v206
	v_mul_f32_e32 v67, v199, v209
	v_mul_f32_e32 v69, v199, v208
	v_fma_f32 v66, v198, v206, -v66
	v_fma_f32 v68, v198, v207, v68
	v_fma_f32 v67, v198, v208, -v67
	v_fma_f32 v69, v198, v209, v69
	v_cvt_pk_f16_f32 v214, v66, v67
	v_cvt_pk_f16_f32 v216, v68, v69
	v_mul_f32_e32 v70, v201, v211
	v_mul_f32_e32 v72, v201, v210
	v_mul_f32_e32 v71, v201, v213
	v_mul_f32_e32 v73, v201, v212
	v_fma_f32 v70, v200, v210, -v70
	v_fma_f32 v72, v200, v211, v72
	v_fma_f32 v71, v200, v212, -v71
	v_fma_f32 v73, v200, v213, v73
	v_cvt_pk_f16_f32 v215, v70, v71
	v_cvt_pk_f16_f32 v217, v72, v73
	v_mul_f32_e32 v66, v203, v207
	v_mul_f32_e32 v68, v203, v206
	v_mul_f32_e32 v67, v203, v209
	v_mul_f32_e32 v69, v203, v208
	v_fma_f32 v66, v202, v206, -v66
	v_fma_f32 v68, v202, v207, v68
	v_fma_f32 v67, v202, v208, -v67
	v_fma_f32 v69, v202, v209, v69
	v_cvt_pk_f16_f32 v218, v66, v67
	v_cvt_pk_f16_f32 v220, v68, v69
	v_mul_f32_e32 v70, v205, v211
	v_mul_f32_e32 v72, v205, v210
	v_mul_f32_e32 v71, v205, v213
	v_mul_f32_e32 v73, v205, v212
	v_fma_f32 v70, v204, v210, -v70
	v_fma_f32 v72, v204, v211, v72
	v_fma_f32 v71, v204, v212, -v71
	v_fma_f32 v73, v204, v213, v73
	v_cvt_pk_f16_f32 v219, v70, v71
	v_cvt_pk_f16_f32 v221, v72, v73
	v_xor_b32_e32 v255, 8, v254
	ds_read2_b64 v[206:209], v255 offset0:0 offset1:16
	ds_read2_b64 v[210:213], v255 offset0:32 offset1:48
	v_mfma_f32_32x32x16_f16 v[2:17], v[190:193], v[214:217], 0
	v_mfma_f32_32x32x16_f16 v[18:33], v[194:197], v[218:221], 0
	s_waitcnt lgkmcnt(0)
	v_mul_f32_e32 v66, v199, v207
	v_mul_f32_e32 v68, v199, v206
	v_mul_f32_e32 v67, v199, v209
	v_mul_f32_e32 v69, v199, v208
	v_fma_f32 v66, v198, v206, -v66
	v_fma_f32 v68, v198, v207, v68
	v_fma_f32 v67, v198, v208, -v67
	v_fma_f32 v69, v198, v209, v69
	v_cvt_pk_f16_f32 v214, v66, v67
	v_cvt_pk_f16_f32 v216, v68, v69
	v_mul_f32_e32 v70, v201, v211
	v_mul_f32_e32 v72, v201, v210
	v_mul_f32_e32 v71, v201, v213
	v_mul_f32_e32 v73, v201, v212
	v_fma_f32 v70, v200, v210, -v70
	v_fma_f32 v72, v200, v211, v72
	v_fma_f32 v71, v200, v212, -v71
	v_fma_f32 v73, v200, v213, v73
	v_cvt_pk_f16_f32 v215, v70, v71
	v_cvt_pk_f16_f32 v217, v72, v73
	v_cvt_pk_f16_f32 v2, v2, v3
	v_cvt_pk_f16_f32 v3, v4, v5
	v_cvt_pk_f16_f32 v4, v6, v7
	v_cvt_pk_f16_f32 v5, v8, v9
	v_cvt_pk_f16_f32 v6, v10, v11
	v_cvt_pk_f16_f32 v7, v12, v13
	v_cvt_pk_f16_f32 v8, v14, v15
	v_cvt_pk_f16_f32 v9, v16, v17
	v_cvt_pk_f16_f32 v18, v18, v19
	v_cvt_pk_f16_f32 v19, v20, v21
	v_cvt_pk_f16_f32 v20, v22, v23
	v_cvt_pk_f16_f32 v21, v24, v25
	v_cvt_pk_f16_f32 v22, v26, v27
	v_cvt_pk_f16_f32 v23, v28, v29
	v_cvt_pk_f16_f32 v24, v30, v31
	v_cvt_pk_f16_f32 v25, v32, v33
	s_setprio 1
	s_waitcnt vmcnt(6)
	v_mul_f32_e32 v66, v203, v207
	v_mul_f32_e32 v68, v203, v206
	v_mfma_f32_32x32x16_f16 v[34:49], v[2:5], v[150:153], 0
	v_mul_f32_e32 v67, v203, v209
	v_mul_f32_e32 v69, v203, v208
	v_mfma_f32_32x32x16_f16 v[34:49], v[18:21], v[146:149], v[34:49]
	v_fma_f32 v66, v202, v206, -v66
	v_fma_f32 v68, v202, v207, v68
	v_mfma_f32_32x32x16_f16 v[34:49], v[6:9], v[142:145], v[34:49]
	v_fma_f32 v67, v202, v208, -v67
	v_fma_f32 v69, v202, v209, v69
	v_mfma_f32_32x32x16_f16 v[34:49], v[22:25], v[138:141], v[34:49]
	v_cvt_pk_f16_f32 v218, v66, v67
	v_cvt_pk_f16_f32 v220, v68, v69
	s_waitcnt vmcnt(2)
	v_mul_f32_e32 v70, v205, v211
	v_mul_f32_e32 v72, v205, v210
	v_mfma_f32_32x32x16_f16 v[50:65], v[2:5], v[134:137], 0
	v_mul_f32_e32 v71, v205, v213
	v_mul_f32_e32 v73, v205, v212
	v_mfma_f32_32x32x16_f16 v[50:65], v[18:21], v[126:129], v[50:65]
	v_fma_f32 v70, v204, v210, -v70
	v_fma_f32 v72, v204, v211, v72
	v_mfma_f32_32x32x16_f16 v[50:65], v[6:9], v[122:125], v[50:65]
	v_fma_f32 v71, v204, v212, -v71
	v_fma_f32 v73, v204, v213, v73
	v_mfma_f32_32x32x16_f16 v[50:65], v[22:25], v[130:133], v[50:65]
	v_cvt_pk_f16_f32 v219, v70, v71
	v_cvt_pk_f16_f32 v221, v72, v73
	v_xor_b32_e32 v255, 16, v254
	ds_read2_b64 v[206:209], v255 offset0:0 offset1:16
	ds_read2_b64 v[210:213], v255 offset0:32 offset1:48
	v_mfma_f32_32x32x16_f16 v[2:17], v[190:193], v[214:217], 0
	v_mfma_f32_32x32x16_f16 v[18:33], v[194:197], v[218:221], 0
	v_cvt_pk_f16_f32 v34, v34, v35
	v_cvt_pk_f16_f32 v35, v36, v37
	v_cvt_pk_f16_f32 v36, v38, v39
	v_cvt_pk_f16_f32 v37, v40, v41
	v_cvt_pk_f16_f32 v38, v42, v43
	v_cvt_pk_f16_f32 v39, v44, v45
	v_cvt_pk_f16_f32 v40, v46, v47
	v_cvt_pk_f16_f32 v41, v48, v49
	v_cvt_pk_f16_f32 v50, v50, v51
	v_cvt_pk_f16_f32 v51, v52, v53
	v_cvt_pk_f16_f32 v52, v54, v55
	v_cvt_pk_f16_f32 v53, v56, v57
	v_cvt_pk_f16_f32 v54, v58, v59
	v_cvt_pk_f16_f32 v55, v60, v61
	v_cvt_pk_f16_f32 v56, v62, v63
	v_cvt_pk_f16_f32 v57, v64, v65
	s_waitcnt vmcnt(2)
	v_cvt_pk_f16_f32 v2, v2, v3
	v_cvt_pk_f16_f32 v3, v4, v5
	v_cvt_pk_f16_f32 v4, v6, v7
	v_cvt_pk_f16_f32 v5, v8, v9
	v_mfma_f32_32x32x16_f16 v[90:105], v[34:37], v[222:225], 0
	v_cvt_pk_f16_f32 v6, v10, v11
	v_cvt_pk_f16_f32 v7, v12, v13
	v_cvt_pk_f16_f32 v8, v14, v15
	v_cvt_pk_f16_f32 v9, v16, v17
	v_mfma_f32_32x32x16_f16 v[106:121], v[34:37], v[238:241], 0
	v_cvt_pk_f16_f32 v18, v18, v19
	v_cvt_pk_f16_f32 v19, v20, v21
	v_cvt_pk_f16_f32 v20, v22, v23
	v_cvt_pk_f16_f32 v21, v24, v25
	v_mfma_f32_32x32x16_f16 v[90:105], v[38:41], v[226:229], v[90:105]
	v_cvt_pk_f16_f32 v22, v26, v27
	v_cvt_pk_f16_f32 v23, v28, v29
	v_cvt_pk_f16_f32 v24, v30, v31
	v_cvt_pk_f16_f32 v25, v32, v33
	v_mfma_f32_32x32x16_f16 v[106:121], v[38:41], v[242:245], v[106:121]
	s_waitcnt lgkmcnt(0)
	v_mul_f32_e32 v66, v199, v207
	v_mul_f32_e32 v68, v199, v206
	v_mul_f32_e32 v67, v199, v209
	v_mfma_f32_32x32x16_f16 v[90:105], v[50:53], v[230:233], v[90:105]
	v_mul_f32_e32 v69, v199, v208
	v_fma_f32 v66, v198, v206, -v66
	v_fma_f32 v68, v198, v207, v68
	v_fma_f32 v67, v198, v208, -v67
	v_mfma_f32_32x32x16_f16 v[106:121], v[50:53], v[246:249], v[106:121]
	v_fma_f32 v69, v198, v209, v69
	v_cvt_pk_f16_f32 v214, v66, v67
	v_cvt_pk_f16_f32 v216, v68, v69
	v_mul_f32_e32 v70, v201, v211
	v_mfma_f32_32x32x16_f16 v[90:105], v[54:57], v[234:237], v[90:105]
	v_mul_f32_e32 v72, v201, v210
	v_mul_f32_e32 v71, v201, v213
	v_mul_f32_e32 v73, v201, v212
	v_fma_f32 v70, v200, v210, -v70
	v_mfma_f32_32x32x16_f16 v[106:121], v[54:57], v[250:253], v[106:121]
	v_fma_f32 v72, v200, v211, v72
	v_fma_f32 v71, v200, v212, -v71
	v_fma_f32 v73, v200, v213, v73
	v_cvt_pk_f16_f32 v215, v70, v71
	v_cvt_pk_f16_f32 v217, v72, v73
	v_mfma_f32_32x32x16_f16 v[34:49], v[2:5], v[150:153], 0
	v_mul_f32_e32 v66, v203, v207
	v_mul_f32_e32 v68, v203, v206
	v_mul_f32_e32 v67, v203, v209
	v_mul_f32_e32 v69, v203, v208
	v_fma_f32 v66, v202, v206, -v66
	v_mfma_f32_32x32x16_f16 v[34:49], v[18:21], v[146:149], v[34:49]
	v_fma_f32 v68, v202, v207, v68
	v_fma_f32 v67, v202, v208, -v67
	v_fma_f32 v69, v202, v209, v69
	v_cvt_pk_f16_f32 v218, v66, v67
	v_cvt_pk_f16_f32 v220, v68, v69
	v_mfma_f32_32x32x16_f16 v[34:49], v[6:9], v[142:145], v[34:49]
	v_mul_f32_e32 v70, v205, v211
	v_mul_f32_e32 v72, v205, v210
	v_mul_f32_e32 v71, v205, v213
	v_mul_f32_e32 v73, v205, v212
	v_fma_f32 v70, v204, v210, -v70
	v_mfma_f32_32x32x16_f16 v[34:49], v[22:25], v[138:141], v[34:49]
	v_fma_f32 v72, v204, v211, v72
	v_fma_f32 v71, v204, v212, -v71
	v_fma_f32 v73, v204, v213, v73
	v_cvt_pk_f16_f32 v219, v70, v71
	v_cvt_pk_f16_f32 v221, v72, v73
	v_mfma_f32_32x32x16_f16 v[50:65], v[2:5], v[134:137], 0
	v_cvt_pk_f16_f32 v90, v90, v91
	v_cvt_pk_f16_f32 v91, v92, v93
	v_cvt_pk_f16_f32 v92, v94, v95
	v_cvt_pk_f16_f32 v93, v96, v97
	v_cvt_pk_f16_f32 v94, v98, v99
	v_mfma_f32_32x32x16_f16 v[50:65], v[18:21], v[126:129], v[50:65]
	v_cvt_pk_f16_f32 v95, v100, v101
	v_cvt_pk_f16_f32 v96, v102, v103
	v_cvt_pk_f16_f32 v97, v104, v105
	v_cvt_pk_f16_f32 v106, v106, v107
	v_cvt_pk_f16_f32 v107, v108, v109
	v_mfma_f32_32x32x16_f16 v[50:65], v[6:9], v[122:125], v[50:65]
	v_cvt_pk_f16_f32 v108, v110, v111
	v_cvt_pk_f16_f32 v109, v112, v113
	v_cvt_pk_f16_f32 v110, v114, v115
	v_cvt_pk_f16_f32 v111, v116, v117
	v_cvt_pk_f16_f32 v112, v118, v119
	v_mfma_f32_32x32x16_f16 v[50:65], v[22:25], v[130:133], v[50:65]
	v_cvt_pk_f16_f32 v113, v120, v121
	ds_write_b128 v173, v[90:93]
	ds_write_b128 v172, v[94:97]
	ds_write_b128 v173, v[106:109] offset:32768
	ds_write_b128 v172, v[110:113] offset:32768
	v_xor_b32_e32 v255, 24, v254
	ds_read2_b64 v[206:209], v255 offset0:0 offset1:16
	ds_read2_b64 v[210:213], v255 offset0:32 offset1:48
	v_mfma_f32_32x32x16_f16 v[2:17], v[190:193], v[214:217], 0
	v_mfma_f32_32x32x16_f16 v[18:33], v[194:197], v[218:221], 0
	v_cvt_pk_f16_f32 v34, v34, v35
	v_cvt_pk_f16_f32 v35, v36, v37
	v_cvt_pk_f16_f32 v36, v38, v39
	v_cvt_pk_f16_f32 v37, v40, v41
	v_cvt_pk_f16_f32 v38, v42, v43
	v_cvt_pk_f16_f32 v39, v44, v45
	v_cvt_pk_f16_f32 v40, v46, v47
	v_cvt_pk_f16_f32 v41, v48, v49
	v_cvt_pk_f16_f32 v50, v50, v51
	v_cvt_pk_f16_f32 v51, v52, v53
	v_cvt_pk_f16_f32 v52, v54, v55
	v_cvt_pk_f16_f32 v53, v56, v57
	v_cvt_pk_f16_f32 v54, v58, v59
	v_cvt_pk_f16_f32 v55, v60, v61
	v_cvt_pk_f16_f32 v56, v62, v63
	v_cvt_pk_f16_f32 v57, v64, v65
	v_mfma_f32_32x32x16_f16 v[90:105], v[34:37], v[222:225], 0
	v_cvt_pk_f16_f32 v2, v2, v3
	v_cvt_pk_f16_f32 v3, v4, v5
	v_cvt_pk_f16_f32 v4, v6, v7
	v_cvt_pk_f16_f32 v5, v8, v9
	v_mfma_f32_32x32x16_f16 v[106:121], v[34:37], v[238:241], 0
	v_cvt_pk_f16_f32 v6, v10, v11
	v_cvt_pk_f16_f32 v7, v12, v13
	v_cvt_pk_f16_f32 v8, v14, v15
	v_cvt_pk_f16_f32 v9, v16, v17
	v_cvt_pk_f16_f32 v18, v18, v19
	v_mfma_f32_32x32x16_f16 v[90:105], v[38:41], v[226:229], v[90:105]
	v_cvt_pk_f16_f32 v19, v20, v21
	v_cvt_pk_f16_f32 v20, v22, v23
	v_cvt_pk_f16_f32 v21, v24, v25
	v_cvt_pk_f16_f32 v22, v26, v27
	v_mfma_f32_32x32x16_f16 v[106:121], v[38:41], v[242:245], v[106:121]
	v_cvt_pk_f16_f32 v23, v28, v29
	v_cvt_pk_f16_f32 v24, v30, v31
	v_cvt_pk_f16_f32 v25, v32, v33
	s_waitcnt lgkmcnt(0)
	v_mul_f32_e32 v66, v199, v207
	v_mfma_f32_32x32x16_f16 v[90:105], v[50:53], v[230:233], v[90:105]
	v_mul_f32_e32 v68, v199, v206
	v_mul_f32_e32 v67, v199, v209
	v_mul_f32_e32 v69, v199, v208
	v_fma_f32 v66, v198, v206, -v66
	v_fma_f32 v68, v198, v207, v68
	v_mfma_f32_32x32x16_f16 v[106:121], v[50:53], v[246:249], v[106:121]
	v_fma_f32 v67, v198, v208, -v67
	v_fma_f32 v69, v198, v209, v69
	v_cvt_pk_f16_f32 v214, v66, v67
	v_cvt_pk_f16_f32 v216, v68, v69
	v_mfma_f32_32x32x16_f16 v[90:105], v[54:57], v[234:237], v[90:105]
	v_mul_f32_e32 v70, v201, v211
	v_mul_f32_e32 v72, v201, v210
	v_mul_f32_e32 v71, v201, v213
	v_mul_f32_e32 v73, v201, v212
	v_fma_f32 v70, v200, v210, -v70
	v_mfma_f32_32x32x16_f16 v[106:121], v[54:57], v[250:253], v[106:121]
	v_fma_f32 v72, v200, v211, v72
	v_fma_f32 v71, v200, v212, -v71
	v_fma_f32 v73, v200, v213, v73
	v_cvt_pk_f16_f32 v215, v70, v71
	v_cvt_pk_f16_f32 v217, v72, v73
	v_mfma_f32_32x32x16_f16 v[34:49], v[2:5], v[150:153], 0
	v_mul_f32_e32 v66, v203, v207
	v_mul_f32_e32 v68, v203, v206
	v_mul_f32_e32 v67, v203, v209
	v_mul_f32_e32 v69, v203, v208
	v_fma_f32 v66, v202, v206, -v66
	v_mfma_f32_32x32x16_f16 v[34:49], v[18:21], v[146:149], v[34:49]
	v_fma_f32 v68, v202, v207, v68
	v_fma_f32 v67, v202, v208, -v67
	v_fma_f32 v69, v202, v209, v69
	v_cvt_pk_f16_f32 v218, v66, v67
	v_cvt_pk_f16_f32 v220, v68, v69
	v_mfma_f32_32x32x16_f16 v[34:49], v[6:9], v[142:145], v[34:49]
	v_mul_f32_e32 v70, v205, v211
	v_mul_f32_e32 v72, v205, v210
	v_mul_f32_e32 v71, v205, v213
	v_mul_f32_e32 v73, v205, v212
	v_fma_f32 v70, v204, v210, -v70
	v_mfma_f32_32x32x16_f16 v[34:49], v[22:25], v[138:141], v[34:49]
	v_fma_f32 v72, v204, v211, v72
	v_fma_f32 v71, v204, v212, -v71
	v_fma_f32 v73, v204, v213, v73
	v_cvt_pk_f16_f32 v219, v70, v71
	v_cvt_pk_f16_f32 v221, v72, v73
	v_cvt_pk_f16_f32 v90, v90, v91
	v_mfma_f32_32x32x16_f16 v[50:65], v[2:5], v[134:137], 0
	v_cvt_pk_f16_f32 v91, v92, v93
	v_cvt_pk_f16_f32 v92, v94, v95
	v_cvt_pk_f16_f32 v93, v96, v97
	v_cvt_pk_f16_f32 v94, v98, v99
	v_cvt_pk_f16_f32 v95, v100, v101
	v_mfma_f32_32x32x16_f16 v[50:65], v[18:21], v[126:129], v[50:65]
	v_cvt_pk_f16_f32 v96, v102, v103
	v_cvt_pk_f16_f32 v97, v104, v105
	v_cvt_pk_f16_f32 v106, v106, v107
	v_cvt_pk_f16_f32 v107, v108, v109
	v_cvt_pk_f16_f32 v108, v110, v111
	v_mfma_f32_32x32x16_f16 v[50:65], v[6:9], v[122:125], v[50:65]
	v_cvt_pk_f16_f32 v109, v112, v113
	v_cvt_pk_f16_f32 v110, v114, v115
	v_cvt_pk_f16_f32 v111, v116, v117
	v_cvt_pk_f16_f32 v112, v118, v119
	v_cvt_pk_f16_f32 v113, v120, v121
	v_mfma_f32_32x32x16_f16 v[50:65], v[22:25], v[130:133], v[50:65]
	v_xor_b32_e32 v74, 0x8a0, v173
	v_xor_b32_e32 v75, 0x8a0, v172
	ds_write_b128 v74, v[90:93]
	ds_write_b128 v75, v[94:97]
	ds_write_b128 v74, v[106:109] offset:32768
	ds_write_b128 v75, v[110:113] offset:32768
	s_nop 0
	v_mfma_f32_32x32x16_f16 v[2:17], v[190:193], v[214:217], 0
	v_mfma_f32_32x32x16_f16 v[18:33], v[194:197], v[218:221], 0
	v_cvt_pk_f16_f32 v34, v34, v35
	v_cvt_pk_f16_f32 v35, v36, v37
	v_cvt_pk_f16_f32 v36, v38, v39
	v_cvt_pk_f16_f32 v37, v40, v41
	v_cvt_pk_f16_f32 v38, v42, v43
	v_cvt_pk_f16_f32 v39, v44, v45
	v_cvt_pk_f16_f32 v40, v46, v47
	v_cvt_pk_f16_f32 v41, v48, v49
	v_cvt_pk_f16_f32 v50, v50, v51
	v_cvt_pk_f16_f32 v51, v52, v53
	v_cvt_pk_f16_f32 v52, v54, v55
	v_cvt_pk_f16_f32 v53, v56, v57
	v_cvt_pk_f16_f32 v54, v58, v59
	v_cvt_pk_f16_f32 v55, v60, v61
	v_cvt_pk_f16_f32 v56, v62, v63
	v_cvt_pk_f16_f32 v57, v64, v65
	v_mfma_f32_32x32x16_f16 v[90:105], v[34:37], v[222:225], 0
	v_cvt_pk_f16_f32 v2, v2, v3
	v_cvt_pk_f16_f32 v3, v4, v5
	v_mfma_f32_32x32x16_f16 v[106:121], v[34:37], v[238:241], 0
	v_cvt_pk_f16_f32 v4, v6, v7
	v_cvt_pk_f16_f32 v5, v8, v9
	v_mfma_f32_32x32x16_f16 v[90:105], v[38:41], v[226:229], v[90:105]
	v_cvt_pk_f16_f32 v6, v10, v11
	v_cvt_pk_f16_f32 v7, v12, v13
	v_mfma_f32_32x32x16_f16 v[106:121], v[38:41], v[242:245], v[106:121]
	v_cvt_pk_f16_f32 v8, v14, v15
	v_cvt_pk_f16_f32 v9, v16, v17
	v_mfma_f32_32x32x16_f16 v[90:105], v[50:53], v[230:233], v[90:105]
	v_cvt_pk_f16_f32 v18, v18, v19
	v_cvt_pk_f16_f32 v19, v20, v21
	v_mfma_f32_32x32x16_f16 v[106:121], v[50:53], v[246:249], v[106:121]
	v_cvt_pk_f16_f32 v20, v22, v23
	v_cvt_pk_f16_f32 v21, v24, v25
	v_mfma_f32_32x32x16_f16 v[90:105], v[54:57], v[234:237], v[90:105]
	v_cvt_pk_f16_f32 v22, v26, v27
	v_cvt_pk_f16_f32 v23, v28, v29
	v_mfma_f32_32x32x16_f16 v[106:121], v[54:57], v[250:253], v[106:121]
	v_cvt_pk_f16_f32 v24, v30, v31
	v_cvt_pk_f16_f32 v25, v32, v33
	v_mfma_f32_32x32x16_f16 v[34:49], v[2:5], v[150:153], 0
	v_mfma_f32_32x32x16_f16 v[34:49], v[18:21], v[146:149], v[34:49]
	v_mfma_f32_32x32x16_f16 v[34:49], v[6:9], v[142:145], v[34:49]
	v_mfma_f32_32x32x16_f16 v[34:49], v[22:25], v[138:141], v[34:49]
	v_mfma_f32_32x32x16_f16 v[50:65], v[2:5], v[134:137], 0
	s_nop 5
	v_cvt_pk_f16_f32 v90, v90, v91
	v_cvt_pk_f16_f32 v91, v92, v93
	v_cvt_pk_f16_f32 v92, v94, v95
	v_cvt_pk_f16_f32 v93, v96, v97
	v_mfma_f32_32x32x16_f16 v[50:65], v[18:21], v[126:129], v[50:65]
	v_cvt_pk_f16_f32 v94, v98, v99
	v_cvt_pk_f16_f32 v95, v100, v101
	v_cvt_pk_f16_f32 v96, v102, v103
	v_cvt_pk_f16_f32 v97, v104, v105
	v_cvt_pk_f16_f32 v106, v106, v107
	v_cvt_pk_f16_f32 v107, v108, v109
	v_mfma_f32_32x32x16_f16 v[50:65], v[6:9], v[122:125], v[50:65]
	v_cvt_pk_f16_f32 v108, v110, v111
	v_cvt_pk_f16_f32 v109, v112, v113
	v_cvt_pk_f16_f32 v110, v114, v115
	v_cvt_pk_f16_f32 v111, v116, v117
	v_cvt_pk_f16_f32 v112, v118, v119
	v_cvt_pk_f16_f32 v113, v120, v121
	v_mfma_f32_32x32x16_f16 v[50:65], v[22:25], v[130:133], v[50:65]
	v_xor_b32_e32 v74, 0x1040, v173
	v_xor_b32_e32 v75, 0x1040, v172
	ds_write_b128 v74, v[90:93]
	ds_write_b128 v75, v[94:97]
	ds_write_b128 v74, v[106:109] offset:32768
	ds_write_b128 v75, v[110:113] offset:32768
	s_nop 11
	v_cvt_pk_f16_f32 v34, v34, v35
	v_cvt_pk_f16_f32 v35, v36, v37
	v_cvt_pk_f16_f32 v36, v38, v39
	v_cvt_pk_f16_f32 v37, v40, v41
	v_cvt_pk_f16_f32 v38, v42, v43
	v_cvt_pk_f16_f32 v39, v44, v45
	v_cvt_pk_f16_f32 v40, v46, v47
	v_cvt_pk_f16_f32 v41, v48, v49
	v_cvt_pk_f16_f32 v50, v50, v51
	v_cvt_pk_f16_f32 v51, v52, v53
	v_cvt_pk_f16_f32 v52, v54, v55
	v_cvt_pk_f16_f32 v53, v56, v57
	v_cvt_pk_f16_f32 v54, v58, v59
	v_cvt_pk_f16_f32 v55, v60, v61
	v_cvt_pk_f16_f32 v56, v62, v63
	v_cvt_pk_f16_f32 v57, v64, v65
	v_mfma_f32_32x32x16_f16 v[90:105], v[34:37], v[222:225], 0
	v_mfma_f32_32x32x16_f16 v[106:121], v[34:37], v[238:241], 0
	v_mfma_f32_32x32x16_f16 v[90:105], v[38:41], v[226:229], v[90:105]
	v_mfma_f32_32x32x16_f16 v[106:121], v[38:41], v[242:245], v[106:121]
	v_mfma_f32_32x32x16_f16 v[90:105], v[50:53], v[230:233], v[90:105]
	v_mfma_f32_32x32x16_f16 v[106:121], v[50:53], v[246:249], v[106:121]
	v_mfma_f32_32x32x16_f16 v[90:105], v[54:57], v[234:237], v[90:105]
	v_mfma_f32_32x32x16_f16 v[106:121], v[54:57], v[250:253], v[106:121]
	v_and_b32_e32 v134, 1, v156
	v_bitop3_b32 v132, v171, s40, v170 bitop3:0x36
	v_bitop3_b32 v131, s41, v154, v160 bitop3:0x36
	v_bitop3_b32 v135, v171, s42, v170 bitop3:0x36
	v_xor_b32_e32 v133, s43, v154
	v_and_b32_e32 v130, 4, v156
	s_lshl_b32 s2, s27, 3
	s_lshl_b32 s3, s5, 2
	s_or_b32 s2, s3, s2
	s_ashr_i32 s3, s2, 31
	s_lshl_b64 s[2:3], s[2:3], 13
	s_add_u32 s2, s20, s2
	s_addc_u32 s3, s21, s3
	v_lshlrev_b32_e32 v154, 1, v169
	v_lshl_add_u64 v[2:3], s[2:3], 0, v[154:155]
	v_add_co_u32_e32 v2, vcc, s23, v2
	s_nop 1
	v_addc_co_u32_e32 v3, vcc, 0, v3, vcc
	v_cvt_pk_f16_f32 v90, v90, v91
	v_cvt_pk_f16_f32 v91, v92, v93
	v_cvt_pk_f16_f32 v92, v94, v95
	v_cvt_pk_f16_f32 v93, v96, v97
	v_cvt_pk_f16_f32 v94, v98, v99
	v_cvt_pk_f16_f32 v95, v100, v101
	v_cvt_pk_f16_f32 v96, v102, v103
	v_cvt_pk_f16_f32 v97, v104, v105
	v_cvt_pk_f16_f32 v106, v106, v107
	v_cvt_pk_f16_f32 v107, v108, v109
	v_cvt_pk_f16_f32 v108, v110, v111
	v_cvt_pk_f16_f32 v109, v112, v113
	v_cvt_pk_f16_f32 v110, v114, v115
	v_cvt_pk_f16_f32 v111, v116, v117
	v_cvt_pk_f16_f32 v112, v118, v119
	v_cvt_pk_f16_f32 v113, v120, v121
	v_xor_b32_e32 v74, 0x18e0, v173
	v_xor_b32_e32 v75, 0x18e0, v172
	ds_write_b128 v74, v[90:93]
	ds_write_b128 v75, v[94:97]
	ds_write_b128 v74, v[106:109] offset:32768
	ds_write_b128 v75, v[110:113] offset:32768
	s_setprio 0
	s_waitcnt lgkmcnt(0)
	s_barrier
	global_load_dwordx4 v[62:65], v154, s[2:3]
	global_load_dwordx4 v[46:49], v154, s[2:3] offset:1024
	global_load_dwordx4 v[42:45], v154, s[2:3] offset:2048
	global_load_dwordx4 v[38:41], v154, s[2:3] offset:3072
	global_load_dwordx4 v[54:57], v[2:3], off offset:1024
	global_load_dwordx4 v[50:53], v[2:3], off offset:2048
	v_lshl_add_u64 v[4:5], s[12:13], 0, v[154:155]
	global_load_dwordx4 v[126:129], v154, s[12:13]
	global_load_dwordx4 v[122:125], v154, s[12:13] offset:1024
	global_load_dwordx4 v[118:121], v154, s[12:13] offset:2048
	global_load_dwordx4 v[114:117], v154, s[12:13] offset:3072
	global_load_dwordx4 v[34:37], v168, s[2:3]
	global_load_dwordx4 v[110:113], v168, s[12:13]
	v_add_co_u32_e32 v4, vcc, s23, v4
	s_nop 1
	v_addc_co_u32_e32 v5, vcc, 0, v5, vcc
	global_load_dwordx4 v[58:61], v[2:3], off offset:3072
	global_load_dwordx4 v[106:109], v[4:5], off offset:1024
	global_load_dwordx4 v[94:97], v[4:5], off offset:2048
	global_load_dwordx4 v[90:93], v[4:5], off offset:3072
	v_bfrev_b32_e32 v3, v156
	v_lshlrev_b32_e32 v7, 5, v167
	v_lshlrev_b32_e32 v6, 9, v167
	v_and_b32_e32 v7, 0x200, v7
	v_lshlrev_b32_e32 v8, 8, v167
	v_lshrrev_b32_e32 v3, 27, v3
	v_lshrrev_b32_e32 v2, 2, v167
	v_lshrrev_b32_e32 v4, 4, v156
	v_xor_b32_e32 v5, v169, v156
	v_and_b32_e32 v6, 0x5800, v6
	v_and_b32_e32 v3, 8, v3
	v_and_or_b32 v7, v8, s24, v7
	v_lshrrev_b32_e32 v5, 1, v5
	v_xor_b32_e32 v4, v2, v4
	v_or3_b32 v3, v7, v6, v3
	v_bitop3_b32 v7, v2, v182, 1 bitop3:0x6c
	v_lshlrev_b32_e32 v2, 1, v167
	v_and_b32_e32 v5, 4, v5
	v_lshlrev_b32_e32 v4, 3, v4
	v_lshrrev_b32_e32 v6, 1, v167
	v_and_b32_e32 v2, 2, v2
	v_and_or_b32 v9, v169, 8, v2
	v_and_b32_e32 v2, 8, v4
	v_and_or_b32 v4, v6, 2, v5
	v_or3_b32 v2, v4, v2, v134
	v_lshlrev_b32_e32 v2, 4, v2
	v_bitop3_b32 v146, v3, s28, v2 bitop3:0x36
	v_xor_b32_e32 v8, v6, v182
	v_xor_b32_e32 v147, 0x2010, v146
	v_lshlrev_b32_e32 v8, 2, v8
	v_and_b32_e32 v8, 4, v8
	v_or3_b32 v6, v9, v7, v8
	v_lshlrev_b32_e32 v7, 11, v167
	v_and_b32_e32 v8, 0x7800, v7
	v_lshlrev_b32_e32 v6, 4, v6
	v_or3_b32 v22, v6, v8, v170
	v_and_b32_e32 v23, 0x8000, v7
	v_xor_b32_e32 v150, 16, v146
	v_xad_u32 v70, v22, s28, v23
	v_xor_b32_e32 v151, 0x2000, v146
	ds_read_b64_tr_b16 v[18:19], v146
	ds_read_b64_tr_b16 v[20:21], v147
	ds_read_b64_tr_b16 v[22:23], v146 offset:32768
	ds_read_b64_tr_b16 v[24:25], v147 offset:32768
	ds_read_b64_tr_b16 v[26:27], v150
	ds_read_b64_tr_b16 v[28:29], v151
	ds_read_b64_tr_b16 v[30:31], v150 offset:32768
	ds_read_b64_tr_b16 v[32:33], v151 offset:32768
	v_xor_b32_e32 v148, 32, v146
	v_xor_b32_e32 v149, 0x2030, v146
	v_xor_b32_e32 v144, 48, v146
	v_xor_b32_e32 v145, 0x2020, v146
	v_xor_b32_e32 v142, 64, v146
	v_xor_b32_e32 v143, 0x2050, v146
	v_xor_b32_e32 v140, 0x50, v146
	v_xor_b32_e32 v141, 0x2040, v146
	v_xor_b32_e32 v138, 0x60, v146
	v_xor_b32_e32 v139, 0x2070, v146
	v_xor_b32_e32 v136, 0x70, v146
	v_xor_b32_e32 v137, 0x2060, v146
	v_xor_b32_e32 v71, 0x60, v70
	s_lshl_b64 s[0:1], s[0:1], 13
	s_add_u32 s0, s8, s0
	s_addc_u32 s1, s9, s1
	s_waitcnt vmcnt(17) lgkmcnt(4)
	v_mfma_f32_32x32x16_f16 v[2:17], v[18:21], v[86:89], 0
	s_waitcnt vmcnt(16)
	v_mfma_f32_32x32x16_f16 v[2:17], v[22:25], v[82:85], v[2:17]
	ds_read_b64_tr_b16 v[206:207], v148
	ds_read_b64_tr_b16 v[208:209], v149
	ds_read_b64_tr_b16 v[210:211], v148 offset:32768
	ds_read_b64_tr_b16 v[212:213], v149 offset:32768
	s_waitcnt lgkmcnt(4)
	v_mfma_f32_32x32x16_f16 v[190:205], v[26:29], v[86:89], 0
	v_mfma_f32_32x32x16_f16 v[190:205], v[30:33], v[82:85], v[190:205]
	s_nop 4
	v_cvt_pk_f16_f32 v2, v2, v3
	v_cvt_pk_f16_f32 v3, v4, v5
	v_cvt_pk_f16_f32 v4, v6, v7
	v_cvt_pk_f16_f32 v5, v8, v9
	v_cvt_pk_f16_f32 v6, v10, v11
	v_cvt_pk_f16_f32 v7, v12, v13
	v_cvt_pk_f16_f32 v8, v14, v15
	v_cvt_pk_f16_f32 v9, v16, v17
	v_xor_b32_e32 v73, 0x280, v70
	ds_write_b128 v70, v[2:5]
	ds_write_b128 v73, v[6:9]
	ds_read_b64_tr_b16 v[18:19], v144
	ds_read_b64_tr_b16 v[20:21], v145
	ds_read_b64_tr_b16 v[22:23], v144 offset:32768
	ds_read_b64_tr_b16 v[24:25], v145 offset:32768
	s_waitcnt lgkmcnt(6)
	v_mfma_f32_32x32x16_f16 v[2:17], v[206:209], v[86:89], 0
	v_mfma_f32_32x32x16_f16 v[2:17], v[210:213], v[82:85], v[2:17]
	v_cvt_pk_f16_f32 v190, v190, v191
	v_cvt_pk_f16_f32 v191, v192, v193
	v_cvt_pk_f16_f32 v192, v194, v195
	v_cvt_pk_f16_f32 v193, v196, v197
	v_cvt_pk_f16_f32 v194, v198, v199
	v_cvt_pk_f16_f32 v195, v200, v201
	v_cvt_pk_f16_f32 v196, v202, v203
	v_cvt_pk_f16_f32 v197, v204, v205
	v_xor_b32_e32 v72, 16, v70
	v_xor_b32_e32 v73, 0x290, v70
	ds_write_b128 v72, v[190:193]
	ds_write_b128 v73, v[194:197]
	ds_read_b64_tr_b16 v[26:27], v142
	ds_read_b64_tr_b16 v[28:29], v143
	ds_read_b64_tr_b16 v[30:31], v142 offset:32768
	ds_read_b64_tr_b16 v[32:33], v143 offset:32768
	s_waitcnt lgkmcnt(6)
	v_mfma_f32_32x32x16_f16 v[190:205], v[18:21], v[86:89], 0
	v_mfma_f32_32x32x16_f16 v[190:205], v[22:25], v[82:85], v[190:205]
	v_cvt_pk_f16_f32 v2, v2, v3
	v_cvt_pk_f16_f32 v3, v4, v5
	v_cvt_pk_f16_f32 v4, v6, v7
	v_cvt_pk_f16_f32 v5, v8, v9
	v_cvt_pk_f16_f32 v6, v10, v11
	v_cvt_pk_f16_f32 v7, v12, v13
	v_cvt_pk_f16_f32 v8, v14, v15
	v_cvt_pk_f16_f32 v9, v16, v17
	v_xor_b32_e32 v72, 32, v70
	v_xor_b32_e32 v73, 0x2a0, v70
	ds_write_b128 v72, v[2:5]
	ds_write_b128 v73, v[6:9]
	ds_read_b64_tr_b16 v[206:207], v140
	ds_read_b64_tr_b16 v[208:209], v141
	ds_read_b64_tr_b16 v[210:211], v140 offset:32768
	ds_read_b64_tr_b16 v[212:213], v141 offset:32768
	s_waitcnt lgkmcnt(6)
	v_mfma_f32_32x32x16_f16 v[2:17], v[26:29], v[86:89], 0
	v_mfma_f32_32x32x16_f16 v[2:17], v[30:33], v[82:85], v[2:17]
	v_cvt_pk_f16_f32 v190, v190, v191
	v_cvt_pk_f16_f32 v191, v192, v193
	v_cvt_pk_f16_f32 v192, v194, v195
	v_cvt_pk_f16_f32 v193, v196, v197
	v_cvt_pk_f16_f32 v194, v198, v199
	v_cvt_pk_f16_f32 v195, v200, v201
	v_cvt_pk_f16_f32 v196, v202, v203
	v_cvt_pk_f16_f32 v197, v204, v205
	v_xor_b32_e32 v72, 48, v70
	v_xor_b32_e32 v73, 0x2b0, v70
	ds_write_b128 v72, v[190:193]
	ds_write_b128 v73, v[194:197]
	ds_read_b64_tr_b16 v[18:19], v138
	ds_read_b64_tr_b16 v[20:21], v139
	ds_read_b64_tr_b16 v[22:23], v138 offset:32768
	ds_read_b64_tr_b16 v[24:25], v139 offset:32768
	s_waitcnt lgkmcnt(6)
	v_mfma_f32_32x32x16_f16 v[190:205], v[206:209], v[86:89], 0
	v_mfma_f32_32x32x16_f16 v[190:205], v[210:213], v[82:85], v[190:205]
	v_cvt_pk_f16_f32 v2, v2, v3
	v_cvt_pk_f16_f32 v3, v4, v5
	v_cvt_pk_f16_f32 v4, v6, v7
	v_cvt_pk_f16_f32 v5, v8, v9
	v_cvt_pk_f16_f32 v6, v10, v11
	v_cvt_pk_f16_f32 v7, v12, v13
	v_cvt_pk_f16_f32 v8, v14, v15
	v_cvt_pk_f16_f32 v9, v16, v17
	v_xor_b32_e32 v72, 64, v70
	v_xor_b32_e32 v73, 0x2c0, v70
	ds_write_b128 v72, v[2:5]
	ds_write_b128 v73, v[6:9]
	ds_read_b64_tr_b16 v[26:27], v136
	ds_read_b64_tr_b16 v[28:29], v137
	ds_read_b64_tr_b16 v[30:31], v136 offset:32768
	ds_read_b64_tr_b16 v[32:33], v137 offset:32768
	s_waitcnt lgkmcnt(6)
	v_mfma_f32_32x32x16_f16 v[2:17], v[18:21], v[86:89], 0
	v_mfma_f32_32x32x16_f16 v[2:17], v[22:25], v[82:85], v[2:17]
	v_cvt_pk_f16_f32 v190, v190, v191
	v_cvt_pk_f16_f32 v191, v192, v193
	v_cvt_pk_f16_f32 v192, v194, v195
	v_cvt_pk_f16_f32 v193, v196, v197
	v_cvt_pk_f16_f32 v194, v198, v199
	v_cvt_pk_f16_f32 v195, v200, v201
	v_cvt_pk_f16_f32 v196, v202, v203
	v_cvt_pk_f16_f32 v197, v204, v205
	v_xor_b32_e32 v72, 0x50, v70
	v_xor_b32_e32 v73, 0x2d0, v70
	ds_write_b128 v72, v[190:193]
	ds_write_b128 v73, v[194:197]
	s_waitcnt lgkmcnt(2)
	v_mfma_f32_32x32x16_f16 v[190:205], v[26:29], v[86:89], 0
	v_mfma_f32_32x32x16_f16 v[190:205], v[30:33], v[82:85], v[190:205]
	v_cvt_pk_f16_f32 v2, v2, v3
	v_cvt_pk_f16_f32 v3, v4, v5
	v_cvt_pk_f16_f32 v4, v6, v7
	v_cvt_pk_f16_f32 v5, v8, v9
	v_cvt_pk_f16_f32 v6, v10, v11
	v_cvt_pk_f16_f32 v7, v12, v13
	v_cvt_pk_f16_f32 v8, v14, v15
	v_cvt_pk_f16_f32 v9, v16, v17
	v_xor_b32_e32 v72, 0x60, v70
	v_xor_b32_e32 v73, 0x2e0, v70
	ds_write_b128 v72, v[2:5]
	ds_write_b128 v73, v[6:9]
	v_cvt_pk_f16_f32 v190, v190, v191
	v_cvt_pk_f16_f32 v191, v192, v193
	v_cvt_pk_f16_f32 v192, v194, v195
	v_cvt_pk_f16_f32 v193, v196, v197
	v_cvt_pk_f16_f32 v194, v198, v199
	v_cvt_pk_f16_f32 v195, v200, v201
	v_cvt_pk_f16_f32 v196, v202, v203
	v_cvt_pk_f16_f32 v197, v204, v205
	v_xor_b32_e32 v72, 0x70, v70
	v_xor_b32_e32 v73, 0x2f0, v70
	ds_write_b128 v72, v[190:193]
	ds_write_b128 v73, v[194:197]
	v_lshl_add_u64 v[2:3], s[0:1], 0, v[154:155]
	v_lshl_add_u64 v[4:5], v[2:3], 0, s[18:19]
	v_add_co_u32_e32 v2, vcc, s25, v2
	s_waitcnt lgkmcnt(0)
	s_nop 0
	v_addc_co_u32_e32 v3, vcc, 0, v3, vcc
	s_barrier
	s_nop 0
	s_nop 0
	global_load_dwordx4 v[102:105], v[2:3], off
	global_load_dwordx4 v[98:101], v[4:5], off offset:1024
	s_setprio 1
	s_add_u32 s0, s2, 0x2000
	s_addc_u32 s1, s3, 0
	v_lshl_add_u64 v[2:3], s[0:1], 0, v[154:155]
	v_add_co_u32_e32 v2, vcc, s23, v2
	global_load_dwordx4 v[66:69], v154, s[0:1]
	global_load_dwordx4 v[70:73], v154, s[0:1] offset:1024
	global_load_dwordx4 v[74:77], v154, s[0:1] offset:2048
	global_load_dwordx4 v[78:81], v154, s[0:1] offset:3072
	v_addc_co_u32_e32 v3, vcc, 0, v3, vcc
	global_load_dwordx4 v[82:85], v168, s[0:1]
	global_load_dwordx4 v[86:89], v[2:3], off offset:1024
	global_load_dwordx4 v[182:185], v[2:3], off offset:2048
	global_load_dwordx4 v[186:189], v[2:3], off offset:3072
	ds_read_b128 v[18:21], v179
	ds_read_b128 v[22:25], v179 offset:32768
	ds_read_b128 v[26:29], v178
	ds_read_b128 v[30:33], v178 offset:32768
	s_add_u32 s0, s2, 0x6000
	s_addc_u32 s1, s3, 0
	s_waitcnt vmcnt(25) lgkmcnt(3)
	v_mfma_f32_32x32x16_f16 v[2:17], v[18:21], v[62:65], 0
	s_add_u32 s2, s2, 0x4000
	s_addc_u32 s3, s3, 0
	s_or_b32 s27, s26, 0x8a0
	s_or_b32 s26, s26, 0xa20
	s_waitcnt vmcnt(24) lgkmcnt(1)
	v_mfma_f32_32x32x16_f16 v[2:17], v[26:29], v[46:49], v[2:17]
	s_waitcnt vmcnt(23)
	v_mfma_f32_32x32x16_f16 v[2:17], v[22:25], v[42:45], v[2:17]
	s_waitcnt vmcnt(22) lgkmcnt(0)
	v_mfma_f32_32x32x16_f16 v[2:17], v[30:33], v[38:41], v[2:17]
	s_waitcnt vmcnt(15)
	v_mfma_f32_32x32x16_f16 v[34:49], v[18:21], v[34:37], 0
	s_nop 9
	v_cvt_pk_f16_f32 v9, v8, v9
	v_cvt_pk_f16_f32 v8, v6, v7
	v_cvt_pk_f16_f32 v7, v4, v5
	v_cvt_pk_f16_f32 v6, v2, v3
	v_cvt_pk_f16_f32 v5, v16, v17
	v_cvt_pk_f16_f32 v4, v14, v15
	v_cvt_pk_f16_f32 v3, v12, v13
	v_mfma_f32_32x32x16_f16 v[34:49], v[26:29], v[54:57], v[34:49]
	v_cvt_pk_f16_f32 v2, v10, v11
	v_mfma_f32_32x32x16_f16 v[34:49], v[22:25], v[50:53], v[34:49]
	s_waitcnt vmcnt(13)
	v_mfma_f32_32x32x16_f16 v[34:49], v[30:33], v[58:61], v[34:49]
	v_mfma_f32_32x32x16_f16 v[18:33], v[6:9], v[126:129], 0
	s_nop 10
	v_cvt_pk_f16_f32 v13, v40, v41
	v_cvt_pk_f16_f32 v12, v38, v39
	v_cvt_pk_f16_f32 v11, v36, v37
	v_cvt_pk_f16_f32 v10, v34, v35
	v_cvt_pk_f16_f32 v17, v48, v49
	v_cvt_pk_f16_f32 v16, v46, v47
	v_cvt_pk_f16_f32 v15, v44, v45
	v_mfma_f32_32x32x16_f16 v[50:65], v[6:9], v[110:113], 0
	v_bitop3_b32 v6, v171, s27, v170 bitop3:0x36
	v_cvt_pk_f16_f32 v14, v42, v43
	v_mfma_f32_32x32x16_f16 v[18:33], v[2:5], v[122:125], v[18:33]
	s_waitcnt vmcnt(12)
	v_mfma_f32_32x32x16_f16 v[50:65], v[2:5], v[106:109], v[50:65]
	ds_read_b128 v[2:5], v6
	ds_read_b128 v[6:9], v6 offset:32768
	v_mfma_f32_32x32x16_f16 v[18:33], v[10:13], v[118:121], v[18:33]
	s_waitcnt vmcnt(11)
	v_mfma_f32_32x32x16_f16 v[50:65], v[10:13], v[94:97], v[50:65]
	s_waitcnt vmcnt(7) lgkmcnt(1)
	v_mfma_f32_32x32x16_f16 v[34:49], v[2:5], v[66:69], 0
	v_mfma_f32_32x32x16_f16 v[18:33], v[14:17], v[114:117], v[18:33]
	v_mfma_f32_32x32x16_f16 v[50:65], v[14:17], v[90:93], v[50:65]
	v_bitop3_b32 v14, v171, s26, v170 bitop3:0x36
	ds_read_b128 v[10:13], v14
	ds_read_b128 v[14:17], v14 offset:32768
	s_nop 7
	v_cvt_pk_f16_f32 v25, v24, v25
	v_cvt_pk_f16_f32 v24, v22, v23
	v_cvt_pk_f16_f32 v23, v20, v21
	v_cvt_pk_f16_f32 v22, v18, v19
	v_cvt_pk_f16_f32 v21, v32, v33
	s_waitcnt vmcnt(6) lgkmcnt(1)
	v_mfma_f32_32x32x16_f16 v[34:49], v[10:13], v[70:73], v[34:49]
	v_cvt_pk_f16_f32 v20, v30, v31
	v_cvt_pk_f16_f32 v19, v28, v29
	v_cvt_pk_f16_f32 v18, v26, v27
	ds_write_b128 v173, v[22:25]
	ds_write_b128 v172, v[18:21]
	v_cvt_pk_f16_f32 v21, v56, v57
	v_cvt_pk_f16_f32 v20, v54, v55
	s_waitcnt vmcnt(5)
	v_mfma_f32_32x32x16_f16 v[34:49], v[6:9], v[74:77], v[34:49]
	v_cvt_pk_f16_f32 v19, v52, v53
	v_cvt_pk_f16_f32 v18, v50, v51
	ds_write_b128 v173, v[18:21] offset:32768
	v_cvt_pk_f16_f32 v21, v64, v65
	v_cvt_pk_f16_f32 v20, v62, v63
	v_cvt_pk_f16_f32 v19, v60, v61
	v_cvt_pk_f16_f32 v18, v58, v59
	s_waitcnt vmcnt(4) lgkmcnt(3)
	v_mfma_f32_32x32x16_f16 v[34:49], v[14:17], v[78:81], v[34:49]
	ds_write_b128 v172, v[18:21] offset:32768
	s_waitcnt vmcnt(3)
	v_mfma_f32_32x32x16_f16 v[66:81], v[2:5], v[82:85], 0
	s_nop 8
	v_cvt_pk_f16_f32 v41, v40, v41
	v_cvt_pk_f16_f32 v40, v38, v39
	v_cvt_pk_f16_f32 v39, v36, v37
	v_cvt_pk_f16_f32 v38, v34, v35
	v_cvt_pk_f16_f32 v85, v48, v49
	v_cvt_pk_f16_f32 v84, v46, v47
	v_cvt_pk_f16_f32 v83, v44, v45
	s_waitcnt vmcnt(2)
	v_mfma_f32_32x32x16_f16 v[66:81], v[10:13], v[86:89], v[66:81]
	v_cvt_pk_f16_f32 v82, v42, v43
	s_waitcnt vmcnt(1)
	v_mfma_f32_32x32x16_f16 v[66:81], v[6:9], v[182:185], v[66:81]
	s_waitcnt vmcnt(0)
	v_mfma_f32_32x32x16_f16 v[66:81], v[14:17], v[186:189], v[66:81]
	v_mfma_f32_32x32x16_f16 v[2:17], v[38:41], v[126:129], 0
	s_nop 10
	v_cvt_pk_f16_f32 v73, v72, v73
	v_cvt_pk_f16_f32 v72, v70, v71
	v_cvt_pk_f16_f32 v70, v66, v67
	v_cvt_pk_f16_f32 v67, v76, v77
	v_cvt_pk_f16_f32 v66, v74, v75
	global_load_dwordx4 v[74:77], v154, s[2:3]
	v_cvt_pk_f16_f32 v71, v68, v69
	v_cvt_pk_f16_f32 v69, v80, v81
	v_cvt_pk_f16_f32 v68, v78, v79
	global_load_dwordx4 v[78:81], v154, s[2:3] offset:1024
	ds_read_b128 v[18:21], v180
	ds_read_b128 v[22:25], v176
	ds_read_b128 v[26:29], v180 offset:32768
	global_load_dwordx4 v[30:33], v154, s[2:3] offset:2048
	v_mfma_f32_32x32x16_f16 v[34:49], v[38:41], v[110:113], 0
	v_mfma_f32_32x32x16_f16 v[2:17], v[82:85], v[122:125], v[2:17]
	v_mfma_f32_32x32x16_f16 v[34:49], v[82:85], v[106:109], v[34:49]
	ds_read_b128 v[82:85], v176 offset:32768
	s_waitcnt vmcnt(2) lgkmcnt(3)
	v_mfma_f32_32x32x16_f16 v[50:65], v[18:21], v[74:77], 0
	v_mfma_f32_32x32x16_f16 v[2:17], v[70:73], v[118:121], v[2:17]
	v_mfma_f32_32x32x16_f16 v[34:49], v[70:73], v[94:97], v[34:49]
	v_lshl_add_u64 v[70:71], s[2:3], 0, v[154:155]
	v_add_co_u32_e32 v152, vcc, s23, v70
	s_nop 1
	v_addc_co_u32_e32 v153, vcc, 0, v71, vcc
	s_waitcnt vmcnt(1) lgkmcnt(2)
	v_mfma_f32_32x32x16_f16 v[50:65], v[22:25], v[78:81], v[50:65]
	v_mfma_f32_32x32x16_f16 v[2:17], v[66:69], v[114:117], v[2:17]
	v_mfma_f32_32x32x16_f16 v[34:49], v[66:69], v[90:93], v[34:49]
	global_load_dwordx4 v[66:69], v154, s[2:3] offset:3072
	s_nop 9
	v_cvt_pk_f16_f32 v9, v8, v9
	v_cvt_pk_f16_f32 v8, v6, v7
	v_cvt_pk_f16_f32 v7, v4, v5
	v_cvt_pk_f16_f32 v6, v2, v3
	v_cvt_pk_f16_f32 v5, v16, v17
	v_cvt_pk_f16_f32 v4, v14, v15
	s_waitcnt vmcnt(1) lgkmcnt(1)
	v_mfma_f32_32x32x16_f16 v[50:65], v[26:29], v[30:33], v[50:65]
	global_load_dwordx4 v[30:33], v168, s[2:3]
	global_load_dwordx4 v[86:89], v[152:153], off offset:1024
	s_nop 0
	global_load_dwordx4 v[168:171], v168, s[0:1]
	v_cvt_pk_f16_f32 v3, v12, v13
	v_cvt_pk_f16_f32 v2, v10, v11
	ds_write_b128 v175, v[6:9]
	ds_write_b128 v174, v[2:5]
	v_cvt_pk_f16_f32 v5, v40, v41
	s_waitcnt vmcnt(3) lgkmcnt(2)
	v_mfma_f32_32x32x16_f16 v[50:65], v[82:85], v[66:69], v[50:65]
	global_load_dwordx4 v[182:185], v154, s[0:1] offset:1024
	v_cvt_pk_f16_f32 v4, v38, v39
	v_cvt_pk_f16_f32 v3, v36, v37
	v_cvt_pk_f16_f32 v2, v34, v35
	ds_write_b128 v175, v[2:5] offset:32768
	v_cvt_pk_f16_f32 v5, v48, v49
	v_cvt_pk_f16_f32 v4, v46, v47
	s_waitcnt vmcnt(3)
	v_mfma_f32_32x32x16_f16 v[66:81], v[18:21], v[30:33], 0
	global_load_dwordx4 v[18:21], v[152:153], off offset:2048
	v_cvt_pk_f16_f32 v3, v44, v45
	v_cvt_pk_f16_f32 v2, v42, v43
	ds_write_b128 v174, v[2:5] offset:32768
	v_cvt_pk_f16_f32 v57, v56, v57
	v_cvt_pk_f16_f32 v56, v54, v55
	v_cvt_pk_f16_f32 v55, v52, v53
	s_waitcnt vmcnt(3)
	v_mfma_f32_32x32x16_f16 v[66:81], v[22:25], v[86:89], v[66:81]
	global_load_dwordx4 v[22:25], v[152:153], off offset:3072
	v_cvt_pk_f16_f32 v54, v50, v51
	s_waitcnt vmcnt(1)
	v_mfma_f32_32x32x16_f16 v[66:81], v[26:29], v[18:21], v[66:81]
	v_lshl_add_u64 v[18:19], s[0:1], 0, v[154:155]
	v_add_co_u32_e32 v152, vcc, s23, v18
	s_nop 1
	v_addc_co_u32_e32 v153, vcc, 0, v19, vcc
	global_load_dwordx4 v[86:89], v[152:153], off offset:1024
	s_waitcnt vmcnt(1)
	v_mfma_f32_32x32x16_f16 v[66:81], v[82:85], v[22:25], v[66:81]
	v_cvt_pk_f16_f32 v85, v64, v65
	v_cvt_pk_f16_f32 v84, v62, v63
	v_cvt_pk_f16_f32 v83, v60, v61
	v_cvt_pk_f16_f32 v82, v58, v59
	v_mfma_f32_32x32x16_f16 v[18:33], v[54:57], v[126:129], 0
	s_nop 6
	v_cvt_pk_f16_f32 v73, v72, v73
	v_cvt_pk_f16_f32 v72, v70, v71
	v_cvt_pk_f16_f32 v70, v66, v67
	v_cvt_pk_f16_f32 v67, v76, v77
	v_cvt_pk_f16_f32 v66, v74, v75
	global_load_dwordx4 v[74:77], v154, s[0:1]
	ds_read_b128 v[2:5], v181
	ds_read_b128 v[6:9], v177
	ds_read_b128 v[10:13], v181 offset:32768
	global_load_dwordx4 v[14:17], v154, s[0:1] offset:2048
	global_load_dwordx4 v[34:37], v154, s[0:1] offset:3072
	v_mfma_f32_32x32x16_f16 v[50:65], v[54:57], v[110:113], 0
	v_cvt_pk_f16_f32 v71, v68, v69
	v_cvt_pk_f16_f32 v69, v80, v81
	v_cvt_pk_f16_f32 v68, v78, v79
	v_mfma_f32_32x32x16_f16 v[18:33], v[82:85], v[122:125], v[18:33]
	v_mfma_f32_32x32x16_f16 v[50:65], v[82:85], v[106:109], v[50:65]
	ds_read_b128 v[82:85], v177 offset:32768
	v_mfma_f32_32x32x16_f16 v[18:33], v[70:73], v[118:121], v[18:33]
	v_mfma_f32_32x32x16_f16 v[50:65], v[70:73], v[94:97], v[50:65]
	v_mfma_f32_32x32x16_f16 v[18:33], v[66:69], v[114:117], v[18:33]
	v_mfma_f32_32x32x16_f16 v[50:65], v[66:69], v[90:93], v[50:65]
	s_nop 10
	v_cvt_pk_f16_f32 v25, v24, v25
	v_cvt_pk_f16_f32 v24, v22, v23
	v_cvt_pk_f16_f32 v23, v20, v21
	v_cvt_pk_f16_f32 v22, v18, v19
	ds_write_b128 v132, v[22:25]
	s_waitcnt vmcnt(2) lgkmcnt(4)
	v_mfma_f32_32x32x16_f16 v[66:81], v[2:5], v[74:77], 0
	s_waitcnt lgkmcnt(3)
	v_mfma_f32_32x32x16_f16 v[66:81], v[6:9], v[182:185], v[66:81]
	s_waitcnt vmcnt(1) lgkmcnt(2)
	v_mfma_f32_32x32x16_f16 v[66:81], v[10:13], v[14:17], v[66:81]
	s_waitcnt vmcnt(0) lgkmcnt(1)
	v_mfma_f32_32x32x16_f16 v[66:81], v[82:85], v[34:37], v[66:81]
	v_mfma_f32_32x32x16_f16 v[34:49], v[2:5], v[168:171], 0
	global_load_dwordx4 v[2:5], v[152:153], off offset:2048
	s_nop 9
	v_cvt_pk_f16_f32 v73, v72, v73
	v_cvt_pk_f16_f32 v72, v70, v71
	v_cvt_pk_f16_f32 v71, v68, v69
	v_cvt_pk_f16_f32 v70, v66, v67
	v_cvt_pk_f16_f32 v69, v80, v81
	v_cvt_pk_f16_f32 v68, v78, v79
	v_mfma_f32_32x32x16_f16 v[34:49], v[6:9], v[86:89], v[34:49]
	global_load_dwordx4 v[6:9], v[152:153], off offset:3072
	v_cvt_pk_f16_f32 v67, v76, v77
	v_cvt_pk_f16_f32 v66, v74, v75
	s_waitcnt vmcnt(1)
	v_mfma_f32_32x32x16_f16 v[34:49], v[10:13], v[2:5], v[34:49]
	s_waitcnt vmcnt(0)
	v_mfma_f32_32x32x16_f16 v[34:49], v[82:85], v[6:9], v[34:49]
	v_mfma_f32_32x32x16_f16 v[2:17], v[70:73], v[126:129], 0
	s_nop 10
	v_cvt_pk_f16_f32 v41, v40, v41
	v_cvt_pk_f16_f32 v40, v38, v39
	v_cvt_pk_f16_f32 v38, v34, v35
	v_cvt_pk_f16_f32 v35, v44, v45
	v_cvt_pk_f16_f32 v34, v42, v43
	v_cvt_pk_f16_f32 v45, v32, v33
	v_cvt_pk_f16_f32 v44, v30, v31
	v_cvt_pk_f16_f32 v43, v28, v29
	v_cvt_pk_f16_f32 v42, v26, v27
	v_mfma_f32_32x32x16_f16 v[18:33], v[70:73], v[110:113], 0
	v_cvt_pk_f16_f32 v39, v36, v37
	v_cvt_pk_f16_f32 v37, v48, v49
	v_cvt_pk_f16_f32 v36, v46, v47
	ds_write_b128 v131, v[42:45]
	v_cvt_pk_f16_f32 v45, v56, v57
	v_cvt_pk_f16_f32 v44, v54, v55
	v_cvt_pk_f16_f32 v43, v52, v53
	v_mfma_f32_32x32x16_f16 v[2:17], v[66:69], v[122:125], v[2:17]
	v_cvt_pk_f16_f32 v42, v50, v51
	ds_write_b128 v132, v[42:45] offset:32768
	v_cvt_pk_f16_f32 v45, v64, v65
	v_cvt_pk_f16_f32 v44, v62, v63
	v_cvt_pk_f16_f32 v43, v60, v61
	v_cvt_pk_f16_f32 v42, v58, v59
	ds_write_b128 v131, v[42:45] offset:32768
	v_mfma_f32_32x32x16_f16 v[18:33], v[66:69], v[106:109], v[18:33]
	v_mfma_f32_32x32x16_f16 v[2:17], v[38:41], v[118:121], v[2:17]
	v_mfma_f32_32x32x16_f16 v[18:33], v[38:41], v[94:97], v[18:33]
	v_mfma_f32_32x32x16_f16 v[2:17], v[34:37], v[114:117], v[2:17]
	v_mfma_f32_32x32x16_f16 v[18:33], v[34:37], v[90:93], v[18:33]
	s_nop 10
	v_cvt_pk_f16_f32 v9, v8, v9
	v_cvt_pk_f16_f32 v8, v6, v7
	v_cvt_pk_f16_f32 v7, v4, v5
	v_cvt_pk_f16_f32 v6, v2, v3
	v_cvt_pk_f16_f32 v5, v16, v17
	v_cvt_pk_f16_f32 v4, v14, v15
	v_cvt_pk_f16_f32 v3, v12, v13
	v_cvt_pk_f16_f32 v2, v10, v11
	ds_write_b128 v135, v[6:9]
	ds_write_b128 v133, v[2:5]
	v_cvt_pk_f16_f32 v5, v24, v25
	v_cvt_pk_f16_f32 v4, v22, v23
	v_cvt_pk_f16_f32 v3, v20, v21
	v_cvt_pk_f16_f32 v2, v18, v19
	ds_write_b128 v135, v[2:5] offset:32768
	v_cvt_pk_f16_f32 v5, v32, v33
	v_cvt_pk_f16_f32 v4, v30, v31
	v_cvt_pk_f16_f32 v3, v28, v29
	v_cvt_pk_f16_f32 v2, v26, v27
	ds_write_b128 v133, v[2:5] offset:32768
	s_setprio 0
	s_waitcnt lgkmcnt(0)
	s_barrier
	s_cmp_lt_i32 s22, 0
	s_cbranch_scc0 .Lno_pref
	s_add_u32 s36, s10, 0x140000
	s_addc_u32 s37, s11, 0
	v_lshlrev_b32_e32 v192, 3, v156
	v_lshlrev_b32_e32 v193, 3, v167
	global_load_dwordx2 v[190:191], v192, s[36:37]
	global_load_dwordx2 v[194:195], v193, s[36:37] offset:2048
